# v26 + P2: first two vmcnt waits of the first K-loop trip after an epilogue relaxed to vmcnt(24) so the 16 epilogue stores stay in flight
# baseline (speedup 1.0000x reference)
.LBB0_159:
	s_cmp_lt_i32 s70, 3
	s_cselect_b64 s[0:1], -1, 0
	s_and_b64 s[0:1], s[0:1], s[2:3]
	s_andn2_b64 vcc, exec, s[0:1]
	s_cbranch_vccnz .LBB0_186
	s_mov_b32 s98, 0
	s_mov_b64 s[2:3], s[94:95]
	s_load_dwordx2 s[4:5], s[2:3], 0x100
	v_mbcnt_lo_u32_b32 v0, -1, 0
	v_mbcnt_hi_u32_b32 v16, -1, v0
	v_mov_b32_e32 v8, v16
	s_and_b32 s2, s97, 0xffffffc0
	s_mov_b32 s3, 0
	s_cmp_gt_u32 s92, 31
	v_add_u32_e32 v6, s2, v8
	s_cbranch_scc1 .LBB0_166
	s_lshl_b32 s2, s92, 13
	s_lshl_b64 s[6:7], s[2:3], 2
	s_waitcnt lgkmcnt(0)
	s_add_u32 s6, s4, s6
	v_lshlrev_b32_e32 v4, 4, v6
	s_addc_u32 s7, s5, s7
	v_ashrrev_i32_e32 v5, 31, v4
	v_lshl_add_u64 v[10:11], v[4:5], 2, s[6:7]
	v_add_co_u32_e32 v0, vcc, 0x12000000, v10
	s_mov_b64 s[6:7], 0x12000000
	s_nop 0
	v_addc_co_u32_e32 v1, vcc, 0, v11, vcc
	global_load_dwordx4 v[0:3], v[0:1], off
	v_lshl_add_u64 v[14:15], v[10:11], 0, s[6:7]
	global_load_dwordx4 v[10:13], v[14:15], off offset:16
	global_load_dwordx4 v[24:27], v[14:15], off offset:32
	global_load_dwordx4 v[28:31], v[14:15], off offset:48
	v_lshl_add_u32 v7, v6, 2, 0
	v_add_u32_e32 v23, 0x23000, v7
	v_cmp_gt_i32_e32 vcc, 64, v6
	s_waitcnt vmcnt(3)
	v_add_f32_e32 v22, v1, v0
	v_add_f32_e32 v21, v2, v22
	v_add_f32_e32 v20, v3, v21
	s_waitcnt vmcnt(2)
	v_add_f32_e32 v19, v10, v20
	v_add_f32_e32 v18, v11, v19
	v_add_f32_e32 v17, v12, v18
	v_add_f32_e32 v15, v13, v17
	s_waitcnt vmcnt(1)
	v_add_f32_e32 v14, v24, v15
	v_add_f32_e32 v13, v25, v14
	v_add_f32_e32 v12, v26, v13
	v_add_f32_e32 v11, v27, v12
	s_waitcnt vmcnt(0)
	v_add_f32_e32 v10, v28, v11
	v_add_f32_e32 v9, v29, v10
	v_add_f32_e32 v7, v30, v9
	v_add_f32_e32 v1, v31, v7
	ds_write_b32 v23, v1
	s_waitcnt lgkmcnt(0)
	s_barrier
	s_and_saveexec_b64 s[6:7], vcc
	s_cbranch_execz .LBB0_163
	v_lshl_add_u32 v2, v6, 5, 0
	v_add_u32_e32 v32, 0x23000, v2
	ds_read_b128 v[24:27], v32
	ds_read_b128 v[28:31], v32 offset:16
	v_and_b32_e32 v33, 64, v16
	v_add_u32_e32 v2, -1, v16
	v_cmp_lt_i32_e32 vcc, v2, v33
	s_nop 1
	v_cndmask_b32_e32 v2, v2, v16, vcc
	v_lshlrev_b32_e32 v34, 2, v2
	s_waitcnt lgkmcnt(1)
	v_add_f32_e32 v2, 0, v24
	v_add_f32_e32 v3, v2, v25
	v_add_f32_e32 v26, v3, v26
	v_add_f32_e32 v27, v26, v27
	s_waitcnt lgkmcnt(0)
	v_add_f32_e32 v28, v27, v28
	v_add_f32_e32 v29, v28, v29
	v_add_f32_e32 v30, v29, v30
	v_add_f32_e32 v31, v30, v31
	ds_bpermute_b32 v24, v34, v31
	v_add_u32_e32 v25, -2, v16
	v_cmp_lt_i32_e32 vcc, v25, v33
	v_add_u32_e32 v34, -4, v16
	s_waitcnt lgkmcnt(0)
	v_add_f32_e32 v24, v31, v24
	v_cndmask_b32_e32 v25, v25, v16, vcc
	v_cmp_gt_i32_e32 vcc, 1, v8
	v_lshlrev_b32_e32 v25, 2, v25
	s_nop 0
	v_cndmask_b32_e32 v24, v24, v31, vcc
	ds_bpermute_b32 v25, v25, v24
	v_cmp_lt_i32_e32 vcc, v34, v33
	s_waitcnt lgkmcnt(0)
	v_add_f32_e32 v25, v24, v25
	v_cndmask_b32_e32 v34, v34, v16, vcc
	v_cmp_gt_i32_e32 vcc, 2, v8
	v_lshlrev_b32_e32 v34, 2, v34
	s_nop 0
	v_cndmask_b32_e32 v24, v25, v24, vcc
	ds_bpermute_b32 v25, v34, v24
	v_add_u32_e32 v34, -8, v16
	v_cmp_lt_i32_e32 vcc, v34, v33
	s_waitcnt lgkmcnt(0)
	v_add_f32_e32 v25, v24, v25
	v_cndmask_b32_e32 v34, v34, v16, vcc
	v_cmp_gt_i32_e32 vcc, 4, v8
	v_lshlrev_b32_e32 v34, 2, v34
	s_nop 0
	v_cndmask_b32_e32 v24, v25, v24, vcc
	ds_bpermute_b32 v25, v34, v24
	v_add_u32_e32 v34, -16, v16
	v_cmp_lt_i32_e32 vcc, v34, v33
	s_waitcnt lgkmcnt(0)
	v_add_f32_e32 v25, v24, v25
	v_cndmask_b32_e32 v34, v34, v16, vcc
	v_cmp_gt_i32_e32 vcc, 8, v8
	v_lshlrev_b32_e32 v34, 2, v34
	s_nop 0
	v_cndmask_b32_e32 v24, v25, v24, vcc
	ds_bpermute_b32 v25, v34, v24
	v_subrev_u32_e32 v34, 32, v16
	v_cmp_lt_i32_e32 vcc, v34, v33
	s_waitcnt lgkmcnt(0)
	v_add_f32_e32 v25, v24, v25
	v_cndmask_b32_e32 v16, v34, v16, vcc
	v_cmp_gt_i32_e32 vcc, 16, v8
	v_lshlrev_b32_e32 v16, 2, v16
	s_nop 0
	v_cndmask_b32_e32 v24, v25, v24, vcc
	ds_bpermute_b32 v16, v16, v24
	v_cmp_gt_i32_e32 vcc, 32, v8
	s_waitcnt lgkmcnt(0)
	v_add_f32_e32 v16, v24, v16
	v_cndmask_b32_e32 v16, v16, v24, vcc
	v_sub_f32_e32 v16, v16, v31
	v_pk_add_f32 v[24:25], v[2:3], v[16:17] op_sel_hi:[1,0]
	v_pk_add_f32 v[26:27], v[26:27], v[16:17] op_sel_hi:[1,0]
	ds_write_b128 v32, v[24:27]
	v_pk_add_f32 v[24:25], v[28:29], v[16:17] op_sel_hi:[1,0]
	v_pk_add_f32 v[26:27], v[30:31], v[16:17] op_sel_hi:[1,0]
	ds_write_b128 v32, v[24:27] offset:16

.LBB0_177:
	s_add_u32 s28, s4, s26
	s_addc_u32 s29, s5, s27
	s_add_u32 s30, s28, 0xe000100
	v_add_u32_e32 v0, s44, v204
	s_addc_u32 s31, s29, 0
	v_add_u32_e32 v1, s44, v205
	ds_read_b128 v[24:27], v0
	ds_read_b128 v[28:31], v1
	v_add_u32_e32 v0, s45, v204
	s_and_b64 s[28:29], s[34:35], exec
	v_add_u32_e32 v1, s45, v205
	ds_read_b128 v[16:19], v0
	ds_read_b128 v[20:23], v1
	v_add_u32_e32 v0, s46, v204
	s_cselect_b32 s29, s7, s31
	s_cselect_b32 s28, s6, s30
	s_add_u32 s61, s56, s26
	v_add_u32_e32 v1, s46, v205
	ds_read_b128 v[8:11], v0
	ds_read_b128 v[12:15], v1
	v_add_u32_e32 v0, s47, v204
	v_add_u32_e32 v4, s47, v205
	s_addc_u32 s62, s57, s27
	ds_read_b128 v[0:3], v0
	ds_read_b128 v[4:7], v4
	s_and_b64 s[30:31], s[34:35], exec
	s_cselect_b32 s31, s23, s62
	s_cselect_b32 s30, s22, s61
	s_add_u32 s61, s58, s26
	s_addc_u32 s62, s59, s27
	s_and_b64 s[34:35], s[34:35], exec
	s_cselect_b32 s35, s25, s62
	s_cselect_b32 s34, s24, s61
	v_lshl_add_u64 v[194:195], v[180:181], 0, s[26:27]
	s_add_i32 m0, s37, 0xc000
	ds_read_b128 v[186:189], v206
	ds_read_b128 v[214:217], v206 offset:2048
	ds_read_b128 v[190:193], v207
	ds_read_b128 v[218:221], v207 offset:2048
	ds_read_b128 v[222:225], v206 offset:4096
	ds_read_b128 v[230:233], v206 offset:6144
	ds_read_b128 v[226:229], v207 offset:4096
	ds_read_b128 v[234:237], v207 offset:6144
	global_load_lds_dwordx4 v[194:195], off
	v_lshl_add_u64 v[194:195], v[178:179], 0, s[26:27]
	s_add_i32 m0, s37, 0xe000
	s_nop 0
	global_load_lds_dwordx4 v[194:195], off
	s_cmp_eq_u32 s98, 0
	s_cbranch_scc0 .Lrlx_p2_a
	s_waitcnt vmcnt(8)
.Lrlx_p2_a:
	s_waitcnt vmcnt(24)
	s_waitcnt lgkmcnt(0)
	s_barrier
	s_setprio 1
	s_waitcnt lgkmcnt(0)
	v_mfma_f32_16x16x128_f8f6f4 v[156:159], v[24:31], v[186:193], v[156:159]
	v_mfma_f32_16x16x128_f8f6f4 v[152:155], v[16:23], v[186:193], v[152:155]
	v_mfma_f32_16x16x128_f8f6f4 v[144:147], v[24:31], v[214:221], v[144:147]
	v_mfma_f32_16x16x128_f8f6f4 v[136:139], v[16:23], v[214:221], v[136:139]
	v_mfma_f32_16x16x128_f8f6f4 v[128:131], v[24:31], v[222:229], v[128:131]
	v_mfma_f32_16x16x128_f8f6f4 v[120:123], v[16:23], v[222:229], v[120:123]
	v_mfma_f32_16x16x128_f8f6f4 v[112:115], v[24:31], v[230:237], v[112:115]
	v_mfma_f32_16x16x128_f8f6f4 v[104:107], v[16:23], v[230:237], v[104:107]
	s_setprio 0
	s_setprio 1
	v_mfma_f32_16x16x128_f8f6f4 v[148:151], v[8:15], v[186:193], v[148:151]
	v_mfma_f32_16x16x128_f8f6f4 v[140:143], v[0:7], v[186:193], v[140:143]
	v_mfma_f32_16x16x128_f8f6f4 v[132:135], v[8:15], v[214:221], v[132:135]
	v_mfma_f32_16x16x128_f8f6f4 v[124:127], v[0:7], v[214:221], v[124:127]
	v_mfma_f32_16x16x128_f8f6f4 v[116:119], v[8:15], v[222:229], v[116:119]
	v_mfma_f32_16x16x128_f8f6f4 v[108:111], v[0:7], v[222:229], v[108:111]
	v_mfma_f32_16x16x128_f8f6f4 v[100:103], v[8:15], v[230:237], v[100:103]
	v_mfma_f32_16x16x128_f8f6f4 v[96:99], v[0:7], v[230:237], v[96:99]
	s_setprio 0
	s_barrier
	s_add_i32 s61, s44, s36
	v_lshl_add_u64 v[186:187], s[30:31], 0, v[160:161]
	s_mov_b32 m0, s61
	ds_read_b128 v[214:217], v206 offset:16384
	ds_read_b128 v[222:225], v206 offset:18432
	ds_read_b128 v[218:221], v207 offset:16384
	ds_read_b128 v[226:229], v207 offset:18432
	ds_read_b128 v[230:233], v206 offset:20480
	ds_read_b128 v[238:241], v206 offset:22528
	ds_read_b128 v[234:237], v207 offset:20480
	ds_read_b128 v[242:245], v207 offset:22528
	global_load_lds_dwordx4 v[186:187], off
	v_lshl_add_u64 v[188:189], s[30:31], 0, v[162:163]
	s_add_i32 m0, s61, 0x2000
	s_add_i32 s30, s46, s36
	global_load_lds_dwordx4 v[188:189], off
	v_lshl_add_u64 v[190:191], s[34:35], 0, v[160:161]
	s_mov_b32 m0, s30
	v_lshl_add_u64 v[192:193], s[34:35], 0, v[162:163]
	global_load_lds_dwordx4 v[190:191], off
	s_add_i32 m0, s30, 0x2000
	v_mov_b32_e32 v173, v165
	global_load_lds_dwordx4 v[192:193], off
	s_mov_b32 m0, s37
	v_lshl_add_u64 v[196:197], s[28:29], 0, v[164:165]
	global_load_lds_dwordx4 v164, s[28:29]
	s_mov_b32 m0, s38
	v_lshl_add_u64 v[194:195], s[28:29], 0, v[172:173]
	global_load_lds_dwordx4 v172, s[28:29]
	s_cmp_eq_u32 s98, 0
	s_cbranch_scc0 .Lrlx_p2_b
	s_waitcnt vmcnt(8)
.Lrlx_p2_b:
	s_waitcnt vmcnt(24)
	s_mov_b32 s98, 0
	s_waitcnt lgkmcnt(0)
	s_barrier
	s_setprio 1
	s_waitcnt lgkmcnt(0)
	v_mfma_f32_16x16x128_f8f6f4 v[92:95], v[24:31], v[214:221], v[92:95]
	v_mfma_f32_16x16x128_f8f6f4 v[88:91], v[16:23], v[214:221], v[88:91]
	v_mfma_f32_16x16x128_f8f6f4 v[80:83], v[24:31], v[222:229], v[80:83]
	v_mfma_f32_16x16x128_f8f6f4 v[72:75], v[16:23], v[222:229], v[72:75]
	v_mfma_f32_16x16x128_f8f6f4 v[64:67], v[24:31], v[230:237], v[64:67]
	v_mfma_f32_16x16x128_f8f6f4 v[56:59], v[16:23], v[230:237], v[56:59]
	v_mfma_f32_16x16x128_f8f6f4 v[48:51], v[24:31], v[238:245], v[48:51]
	v_mfma_f32_16x16x128_f8f6f4 v[40:43], v[16:23], v[238:245], v[40:43]
	s_setprio 0
	s_setprio 1
	v_mfma_f32_16x16x128_f8f6f4 v[84:87], v[8:15], v[214:221], v[84:87]
	v_mfma_f32_16x16x128_f8f6f4 v[76:79], v[0:7], v[214:221], v[76:79]
	v_mfma_f32_16x16x128_f8f6f4 v[68:71], v[8:15], v[222:229], v[68:71]
	v_mfma_f32_16x16x128_f8f6f4 v[60:63], v[0:7], v[222:229], v[60:63]
	v_mfma_f32_16x16x128_f8f6f4 v[52:55], v[8:15], v[230:237], v[52:55]
	v_mfma_f32_16x16x128_f8f6f4 v[44:47], v[0:7], v[230:237], v[44:47]
	v_mfma_f32_16x16x128_f8f6f4 v[36:39], v[8:15], v[238:245], v[36:39]
	v_mfma_f32_16x16x128_f8f6f4 v[32:35], v[0:7], v[238:245], v[32:35]
	s_setprio 0
	s_barrier
	s_add_i32 s30, 0, 0x18000
	s_add_i32 s31, 0, 0x1c000
	v_add_u32_e32 v0, s30, v204
	v_add_u32_e32 v4, s30, v205
	v_add_u32_e32 v8, s48, v204
	v_add_u32_e32 v12, s48, v205
	v_add_u32_e32 v16, s31, v204
	v_add_u32_e32 v20, s31, v205
	v_add_u32_e32 v24, s49, v204
	v_add_u32_e32 v28, s49, v205
	ds_read_b128 v[0:3], v0
	ds_read_b128 v[4:7], v4
	ds_read_b128 v[8:11], v8
	ds_read_b128 v[12:15], v12
	ds_read_b128 v[16:19], v16
	ds_read_b128 v[20:23], v20
	ds_read_b128 v[24:27], v24
	ds_read_b128 v[28:31], v28
	s_mov_b32 m0, s39
	v_lshl_add_u64 v[184:185], s[28:29], 0, v[184:185]
	ds_read_b128 v[214:217], v206 offset:32768
	ds_read_b128 v[222:225], v206 offset:34816
	ds_read_b128 v[218:221], v207 offset:32768
	ds_read_b128 v[226:229], v207 offset:34816
	ds_read_b128 v[230:233], v206 offset:36864
	ds_read_b128 v[238:241], v206 offset:38912
	ds_read_b128 v[234:237], v207 offset:36864
	ds_read_b128 v[242:245], v207 offset:38912
	global_load_lds_dwordx4 v[184:185], off
	v_lshl_add_u64 v[182:183], s[28:29], 0, v[182:183]
	s_mov_b32 m0, s40
	s_nop 0
	global_load_lds_dwordx4 v[182:183], off
	s_waitcnt vmcnt(8)
	s_waitcnt lgkmcnt(0)
	s_barrier
	s_setprio 1
	s_waitcnt lgkmcnt(0)
	v_mfma_f32_16x16x128_f8f6f4 v[156:159], v[0:7], v[214:221], v[156:159]
	v_mfma_f32_16x16x128_f8f6f4 v[152:155], v[8:15], v[214:221], v[152:155]
	v_mfma_f32_16x16x128_f8f6f4 v[144:147], v[0:7], v[222:229], v[144:147]
	v_mfma_f32_16x16x128_f8f6f4 v[136:139], v[8:15], v[222:229], v[136:139]
	v_mfma_f32_16x16x128_f8f6f4 v[128:131], v[0:7], v[230:237], v[128:131]
	v_mfma_f32_16x16x128_f8f6f4 v[120:123], v[8:15], v[230:237], v[120:123]
	v_mfma_f32_16x16x128_f8f6f4 v[112:115], v[0:7], v[238:245], v[112:115]
	v_mfma_f32_16x16x128_f8f6f4 v[104:107], v[8:15], v[238:245], v[104:107]
	s_setprio 0
	s_setprio 1
	v_mfma_f32_16x16x128_f8f6f4 v[148:151], v[16:23], v[214:221], v[148:151]
	v_mfma_f32_16x16x128_f8f6f4 v[140:143], v[24:31], v[214:221], v[140:143]
	v_mfma_f32_16x16x128_f8f6f4 v[132:135], v[16:23], v[222:229], v[132:135]
	v_mfma_f32_16x16x128_f8f6f4 v[124:127], v[24:31], v[222:229], v[124:127]
	v_mfma_f32_16x16x128_f8f6f4 v[116:119], v[16:23], v[230:237], v[116:119]
	v_mfma_f32_16x16x128_f8f6f4 v[108:111], v[24:31], v[230:237], v[108:111]
	v_mfma_f32_16x16x128_f8f6f4 v[100:103], v[16:23], v[238:245], v[100:103]
	v_mfma_f32_16x16x128_f8f6f4 v[96:99], v[24:31], v[238:245], v[96:99]
	s_setprio 0
	s_barrier
	s_add_i32 s28, s30, s36
	v_lshl_add_u64 v[182:183], v[186:187], 0, s[14:15]
	s_mov_b32 m0, s28
	ds_read_b128 v[214:217], v206 offset:49152
	ds_read_b128 v[222:225], v206 offset:51200
	ds_read_b128 v[218:221], v207 offset:49152
	ds_read_b128 v[226:229], v207 offset:51200
	ds_read_b128 v[230:233], v206 offset:53248
	ds_read_b128 v[238:241], v206 offset:55296
	ds_read_b128 v[234:237], v207 offset:53248
	ds_read_b128 v[242:245], v207 offset:55296
	global_load_lds_dwordx4 v[182:183], off
	v_lshl_add_u64 v[182:183], v[188:189], 0, s[14:15]
	s_add_i32 m0, s28, 0x2000
	s_add_i32 s28, s31, s36
	global_load_lds_dwordx4 v[182:183], off
	v_lshl_add_u64 v[182:183], v[190:191], 0, s[14:15]
	s_mov_b32 m0, s28
	s_nop 0
	global_load_lds_dwordx4 v[182:183], off
	v_lshl_add_u64 v[182:183], v[192:193], 0, s[14:15]
	s_add_i32 m0, s28, 0x2000
	s_nop 0
	global_load_lds_dwordx4 v[182:183], off
	v_lshl_add_u64 v[182:183], v[196:197], 0, s[14:15]
	s_mov_b32 m0, s41
	s_nop 0
	global_load_lds_dwordx4 v[182:183], off
	v_lshl_add_u64 v[182:183], v[194:195], 0, s[14:15]
	s_mov_b32 m0, s42
	s_nop 0
	global_load_lds_dwordx4 v[182:183], off
	s_waitcnt vmcnt(8)
	s_waitcnt lgkmcnt(0)
	s_barrier
	s_setprio 1
	s_waitcnt lgkmcnt(0)
	v_mfma_f32_16x16x128_f8f6f4 v[92:95], v[0:7], v[214:221], v[92:95]
	v_mfma_f32_16x16x128_f8f6f4 v[88:91], v[8:15], v[214:221], v[88:91]
	v_mfma_f32_16x16x128_f8f6f4 v[80:83], v[0:7], v[222:229], v[80:83]
	v_mfma_f32_16x16x128_f8f6f4 v[72:75], v[8:15], v[222:229], v[72:75]
	v_mfma_f32_16x16x128_f8f6f4 v[64:67], v[0:7], v[230:237], v[64:67]
	v_mfma_f32_16x16x128_f8f6f4 v[56:59], v[8:15], v[230:237], v[56:59]
	v_mfma_f32_16x16x128_f8f6f4 v[48:51], v[0:7], v[238:245], v[48:51]
	v_mfma_f32_16x16x128_f8f6f4 v[40:43], v[8:15], v[238:245], v[40:43]
	s_setprio 0
	s_setprio 1
	v_mfma_f32_16x16x128_f8f6f4 v[84:87], v[16:23], v[214:221], v[84:87]
	v_mfma_f32_16x16x128_f8f6f4 v[76:79], v[24:31], v[214:221], v[76:79]
	v_mfma_f32_16x16x128_f8f6f4 v[68:71], v[16:23], v[222:229], v[68:71]
	v_mfma_f32_16x16x128_f8f6f4 v[60:63], v[24:31], v[222:229], v[60:63]
	v_mfma_f32_16x16x128_f8f6f4 v[52:55], v[16:23], v[230:237], v[52:55]
	v_mfma_f32_16x16x128_f8f6f4 v[44:47], v[24:31], v[230:237], v[44:47]
	v_mfma_f32_16x16x128_f8f6f4 v[36:39], v[16:23], v[238:245], v[36:39]
	v_mfma_f32_16x16x128_f8f6f4 v[32:35], v[24:31], v[238:245], v[32:35]
	s_setprio 0
	s_barrier
	s_add_i32 s60, s60, 2
	s_add_u32 s26, s26, 0x100
	s_addc_u32 s27, s27, 0
	s_cmp_gt_u32 s60, 5
	s_cbranch_scc1 .LBB0_180

.LBB0_180:
	s_mov_b32 s98, 1
	s_and_b64 vcc, exec, s[18:19]
	s_cbranch_vccz .LBB0_182
	s_barrier

	.amdhsa_kernel _Z6mk_fwd4Args
		.amdhsa_group_segment_fixed_size 0
		.amdhsa_private_segment_fixed_size 0
		.amdhsa_kernarg_size 528
		.amdhsa_user_sgpr_count 2
		.amdhsa_user_sgpr_dispatch_ptr 0
		.amdhsa_user_sgpr_queue_ptr 0
		.amdhsa_user_sgpr_kernarg_segment_ptr 1
		.amdhsa_user_sgpr_dispatch_id 0
		.amdhsa_user_sgpr_kernarg_preload_length 0
		.amdhsa_user_sgpr_kernarg_preload_offset 0
		.amdhsa_user_sgpr_private_segment_size 0
		.amdhsa_uses_dynamic_stack 0
		.amdhsa_enable_private_segment 0
		.amdhsa_system_sgpr_workgroup_id_x 1
		.amdhsa_system_sgpr_workgroup_id_y 0
		.amdhsa_system_sgpr_workgroup_id_z 0
		.amdhsa_system_sgpr_workgroup_info 0
		.amdhsa_system_vgpr_workitem_id 0
		.amdhsa_next_free_vgpr 256
		.amdhsa_next_free_sgpr 99
		.amdhsa_accum_offset 256
		.amdhsa_reserve_vcc 1
		.amdhsa_float_round_mode_32 0
		.amdhsa_float_round_mode_16_64 0
		.amdhsa_float_denorm_mode_32 3
		.amdhsa_float_denorm_mode_16_64 3
		.amdhsa_dx10_clamp 1
		.amdhsa_ieee_mode 1
		.amdhsa_fp16_overflow 0
		.amdhsa_tg_split 0
		.amdhsa_exception_fp_ieee_invalid_op 0
		.amdhsa_exception_fp_denorm_src 0
		.amdhsa_exception_fp_ieee_div_zero 0
		.amdhsa_exception_fp_ieee_overflow 0
		.amdhsa_exception_fp_ieee_underflow 0
		.amdhsa_exception_fp_ieee_inexact 0
		.amdhsa_exception_int_div_zero 0
	.end_amdhsa_kernel

amdhsa.kernels:
  - .agpr_count:     0
    .args:
      - .offset:         0
        .size:           272
        .value_kind:     by_value
      - .offset:         272
        .size:           4
        .value_kind:     hidden_block_count_x
      - .offset:         276
        .size:           4
        .value_kind:     hidden_block_count_y
      - .offset:         280
        .size:           4
        .value_kind:     hidden_block_count_z
      - .offset:         284
        .size:           2
        .value_kind:     hidden_group_size_x
      - .offset:         286
        .size:           2
        .value_kind:     hidden_group_size_y
      - .offset:         288
        .size:           2
        .value_kind:     hidden_group_size_z
      - .offset:         290
        .size:           2
        .value_kind:     hidden_remainder_x
      - .offset:         292
        .size:           2
        .value_kind:     hidden_remainder_y
      - .offset:         294
        .size:           2
        .value_kind:     hidden_remainder_z
      - .offset:         312
        .size:           8
        .value_kind:     hidden_global_offset_x
      - .offset:         320
        .size:           8
        .value_kind:     hidden_global_offset_y
      - .offset:         328
        .size:           8
        .value_kind:     hidden_global_offset_z
      - .offset:         336
        .size:           2
        .value_kind:     hidden_grid_dims
      - .offset:         392
        .size:           4
        .value_kind:     hidden_dynamic_lds_size
    .group_segment_fixed_size: 0
    .kernarg_segment_align: 8
    .kernarg_segment_size: 528
    .language:       OpenCL C
    .language_version:
      - 2
      - 0
    .max_flat_workgroup_size: 512
    .name:           _Z6mk_fwd4Args
    .private_segment_fixed_size: 0
    .sgpr_count:     105
    .sgpr_spill_count: 80
    .symbol:         _Z6mk_fwd4Args.kd
    .uniform_work_group_size: 1
    .uses_dynamic_stack: false
    .vgpr_count:     256
    .vgpr_spill_count: 0
    .wavefront_size: 64
